# v10 + router pass A: the four token rows of a wave loaded together instead of one after another behind each wave reduction
# baseline (speedup 1.0000x reference)
.LBB0_568:
	s_and_saveexec_b64 s[2:3], s[0:1]
	ds_write_b32 v57, v19 offset:37252
	s_or_b64 exec, exec, s[2:3]
	s_lshl_b32 s8, s33, 5
	s_add_i32 s2, s8, s14
	s_ashr_i32 s3, s2, 31
	s_lshl_b64 s[6:7], s[2:3], 12
	v_lshl_add_u64 v[12:13], v[20:21], 0, s[6:7]
	global_load_dwordx4 v[0:3], v[12:13], off
	global_load_dwordx4 v[4:7], v[12:13], off offset:1024
	global_load_dwordx4 v[8:11], v[12:13], off offset:2048
	s_nop 0
	global_load_dwordx4 v[12:15], v[12:13], off offset:3072
	s_or_b32 s4, s2, 1
	s_ashr_i32 s5, s4, 31
	s_lshl_b64 s[4:5], s[4:5], 12
	v_lshl_add_u64 v[208:209], v[20:21], 0, s[4:5]
	global_load_dwordx4 v[160:163], v[208:209], off
	global_load_dwordx4 v[164:167], v[208:209], off offset:1024
	global_load_dwordx4 v[168:171], v[208:209], off offset:2048
	global_load_dwordx4 v[172:175], v[208:209], off offset:3072
	s_or_b32 s4, s2, 2
	s_ashr_i32 s5, s4, 31
	s_lshl_b64 s[4:5], s[4:5], 12
	v_lshl_add_u64 v[208:209], v[20:21], 0, s[4:5]
	global_load_dwordx4 v[176:179], v[208:209], off
	global_load_dwordx4 v[180:183], v[208:209], off offset:1024
	global_load_dwordx4 v[184:187], v[208:209], off offset:2048
	global_load_dwordx4 v[188:191], v[208:209], off offset:3072
	s_or_b32 s4, s2, 3
	s_ashr_i32 s5, s4, 31
	s_lshl_b64 s[4:5], s[4:5], 12
	v_lshl_add_u64 v[208:209], v[20:21], 0, s[4:5]
	global_load_dwordx4 v[192:195], v[208:209], off
	global_load_dwordx4 v[196:199], v[208:209], off offset:1024
	global_load_dwordx4 v[200:203], v[208:209], off offset:2048
	global_load_dwordx4 v[204:207], v[208:209], off offset:3072
	s_waitcnt vmcnt(15)
	v_lshlrev_b32_e32 v18, 16, v0
	v_and_b32_e32 v0, 0xffff0000, v0
	v_lshlrev_b32_e32 v30, 16, v1
	v_and_b32_e32 v1, 0xffff0000, v1
	v_lshlrev_b32_e32 v31, 16, v2
	v_and_b32_e32 v2, 0xffff0000, v2
	v_mul_f32_e32 v0, v0, v0
	v_mul_f32_e32 v1, v1, v1
	v_lshlrev_b32_e32 v32, 16, v3
	v_and_b32_e32 v3, 0xffff0000, v3
	v_mul_f32_e32 v2, v2, v2
	v_fmac_f32_e32 v0, v18, v18
	v_fmac_f32_e32 v1, v30, v30
	s_waitcnt vmcnt(14)
	v_lshlrev_b32_e32 v33, 16, v4
	v_and_b32_e32 v4, 0xffff0000, v4
	v_mul_f32_e32 v3, v3, v3
	v_fmac_f32_e32 v2, v31, v31
	v_add_f32_e32 v0, v0, v1
	v_lshlrev_b32_e32 v34, 16, v5
	v_and_b32_e32 v5, 0xffff0000, v5
	v_mul_f32_e32 v4, v4, v4
	v_fmac_f32_e32 v3, v32, v32
	v_add_f32_e32 v0, v2, v0
	v_lshlrev_b32_e32 v35, 16, v6
	v_and_b32_e32 v6, 0xffff0000, v6
	v_mul_f32_e32 v5, v5, v5
	v_fmac_f32_e32 v4, v33, v33
	v_add_f32_e32 v0, v3, v0
	v_lshlrev_b32_e32 v36, 16, v7
	v_and_b32_e32 v7, 0xffff0000, v7
	v_mul_f32_e32 v6, v6, v6
	v_fmac_f32_e32 v5, v34, v34
	v_add_f32_e32 v0, v4, v0
	s_waitcnt vmcnt(13)
	v_lshlrev_b32_e32 v37, 16, v8
	v_and_b32_e32 v8, 0xffff0000, v8
	v_mul_f32_e32 v7, v7, v7
	v_fmac_f32_e32 v6, v35, v35
	v_add_f32_e32 v0, v5, v0
	v_lshlrev_b32_e32 v38, 16, v9
	v_and_b32_e32 v9, 0xffff0000, v9
	v_mul_f32_e32 v8, v8, v8
	v_fmac_f32_e32 v7, v36, v36
	v_add_f32_e32 v0, v6, v0
	v_lshlrev_b32_e32 v39, 16, v10
	v_and_b32_e32 v10, 0xffff0000, v10
	v_mul_f32_e32 v9, v9, v9
	v_fmac_f32_e32 v8, v37, v37
	v_add_f32_e32 v0, v7, v0
	v_lshlrev_b32_e32 v40, 16, v11
	v_and_b32_e32 v11, 0xffff0000, v11
	v_mul_f32_e32 v10, v10, v10
	v_fmac_f32_e32 v9, v38, v38
	v_add_f32_e32 v0, v8, v0
	s_waitcnt vmcnt(12)
	v_lshlrev_b32_e32 v41, 16, v12
	v_and_b32_e32 v12, 0xffff0000, v12
	v_mul_f32_e32 v11, v11, v11
	v_fmac_f32_e32 v10, v39, v39
	v_add_f32_e32 v0, v9, v0
	v_lshlrev_b32_e32 v42, 16, v13
	v_and_b32_e32 v13, 0xffff0000, v13
	v_mul_f32_e32 v12, v12, v12
	v_fmac_f32_e32 v11, v40, v40
	v_add_f32_e32 v0, v10, v0
	v_lshlrev_b32_e32 v43, 16, v14
	v_and_b32_e32 v14, 0xffff0000, v14
	v_mul_f32_e32 v13, v13, v13
	v_fmac_f32_e32 v12, v41, v41
	v_add_f32_e32 v0, v11, v0
	v_lshlrev_b32_e32 v44, 16, v15
	v_and_b32_e32 v15, 0xffff0000, v15
	v_mul_f32_e32 v14, v14, v14
	v_fmac_f32_e32 v13, v42, v42
	v_add_f32_e32 v0, v12, v0
	v_mul_f32_e32 v15, v15, v15
	v_fmac_f32_e32 v14, v43, v43
	v_add_f32_e32 v0, v13, v0
	v_add_f32_e32 v0, v14, v0
	v_fmac_f32_e32 v15, v44, v44
	v_add_f32_e32 v0, v15, v0
	ds_bpermute_b32 v1, v58, v0
	s_waitcnt lgkmcnt(0)
	v_add_f32_e32 v0, v0, v1
	ds_bpermute_b32 v1, v59, v0
	s_waitcnt lgkmcnt(0)
	v_add_f32_e32 v0, v0, v1
	ds_bpermute_b32 v1, v60, v0
	s_waitcnt lgkmcnt(0)
	v_add_f32_e32 v0, v0, v1
	ds_bpermute_b32 v1, v61, v0
	s_waitcnt lgkmcnt(0)
	v_add_f32_e32 v0, v0, v1
	ds_bpermute_b32 v1, v62, v0
	s_waitcnt lgkmcnt(0)
	v_add_f32_e32 v0, v0, v1
	ds_bpermute_b32 v1, v63, v0
	s_and_saveexec_b64 s[6:7], s[66:67]
	s_cbranch_execz .LBB0_572
	s_waitcnt lgkmcnt(0)
	v_add_f32_e32 v0, v0, v1
	v_fmamk_f32 v0, v0, 0x3a000000, v69
	v_mul_f32_e32 v1, 0x4b800000, v0
	v_cmp_gt_f32_e32 vcc, s52, v0
	s_nop 1
	v_cndmask_b32_e32 v0, v0, v1, vcc
	v_rsq_f32_e32 v0, v0
	s_nop 0
	v_mul_f32_e32 v1, 0x45800000, v0
	v_cndmask_b32_e32 v0, v0, v1, vcc
	v_mov_b32_e32 v1, s96
	ds_write_b32 v1, v0
.LBB0_572:
	s_or_b64 exec, exec, s[6:7]
	s_or_b32 s6, s2, 1
	s_ashr_i32 s7, s6, 31
	s_lshl_b64 s[6:7], s[6:7], 12
	s_waitcnt lgkmcnt(0)
	s_waitcnt vmcnt(11)
	v_lshlrev_b32_e32 v18, 16, v160
	v_and_b32_e32 v160, 0xffff0000, v160
	v_lshlrev_b32_e32 v30, 16, v161
	v_and_b32_e32 v161, 0xffff0000, v161
	v_lshlrev_b32_e32 v31, 16, v162
	v_and_b32_e32 v162, 0xffff0000, v162
	v_mul_f32_e32 v160, v160, v160
	v_mul_f32_e32 v161, v161, v161
	v_lshlrev_b32_e32 v32, 16, v163
	v_and_b32_e32 v163, 0xffff0000, v163
	v_mul_f32_e32 v162, v162, v162
	v_fmac_f32_e32 v160, v18, v18
	v_fmac_f32_e32 v161, v30, v30
	s_waitcnt vmcnt(10)
	v_lshlrev_b32_e32 v33, 16, v164
	v_and_b32_e32 v164, 0xffff0000, v164
	v_mul_f32_e32 v163, v163, v163
	v_fmac_f32_e32 v162, v31, v31
	v_add_f32_e32 v160, v160, v161
	v_lshlrev_b32_e32 v34, 16, v165
	v_and_b32_e32 v165, 0xffff0000, v165
	v_mul_f32_e32 v164, v164, v164
	v_fmac_f32_e32 v163, v32, v32
	v_add_f32_e32 v160, v162, v160
	v_lshlrev_b32_e32 v35, 16, v166
	v_and_b32_e32 v166, 0xffff0000, v166
	v_mul_f32_e32 v165, v165, v165
	v_fmac_f32_e32 v164, v33, v33
	v_add_f32_e32 v160, v163, v160
	v_lshlrev_b32_e32 v36, 16, v167
	v_and_b32_e32 v167, 0xffff0000, v167
	v_mul_f32_e32 v166, v166, v166
	v_fmac_f32_e32 v165, v34, v34
	v_add_f32_e32 v160, v164, v160
	s_waitcnt vmcnt(9)
	v_lshlrev_b32_e32 v37, 16, v168
	v_and_b32_e32 v168, 0xffff0000, v168
	v_mul_f32_e32 v167, v167, v167
	v_fmac_f32_e32 v166, v35, v35
	v_add_f32_e32 v160, v165, v160
	v_lshlrev_b32_e32 v38, 16, v169
	v_and_b32_e32 v169, 0xffff0000, v169
	v_mul_f32_e32 v168, v168, v168
	v_fmac_f32_e32 v167, v36, v36
	v_add_f32_e32 v160, v166, v160
	v_lshlrev_b32_e32 v39, 16, v170
	v_and_b32_e32 v170, 0xffff0000, v170
	v_mul_f32_e32 v169, v169, v169
	v_fmac_f32_e32 v168, v37, v37
	v_add_f32_e32 v160, v167, v160
	v_lshlrev_b32_e32 v40, 16, v171
	v_and_b32_e32 v171, 0xffff0000, v171
	v_mul_f32_e32 v170, v170, v170
	v_fmac_f32_e32 v169, v38, v38
	v_add_f32_e32 v160, v168, v160
	s_waitcnt vmcnt(8)
	v_lshlrev_b32_e32 v41, 16, v172
	v_and_b32_e32 v172, 0xffff0000, v172
	v_mul_f32_e32 v171, v171, v171
	v_fmac_f32_e32 v170, v39, v39
	v_add_f32_e32 v160, v169, v160
	v_lshlrev_b32_e32 v42, 16, v173
	v_and_b32_e32 v173, 0xffff0000, v173
	v_mul_f32_e32 v172, v172, v172
	v_fmac_f32_e32 v171, v40, v40
	v_add_f32_e32 v160, v170, v160
	v_lshlrev_b32_e32 v43, 16, v174
	v_and_b32_e32 v174, 0xffff0000, v174
	v_mul_f32_e32 v173, v173, v173
	v_fmac_f32_e32 v172, v41, v41
	v_add_f32_e32 v160, v171, v160
	v_lshlrev_b32_e32 v44, 16, v175
	v_and_b32_e32 v175, 0xffff0000, v175
	v_mul_f32_e32 v174, v174, v174
	v_fmac_f32_e32 v173, v42, v42
	v_add_f32_e32 v160, v172, v160
	v_mul_f32_e32 v175, v175, v175
	v_fmac_f32_e32 v174, v43, v43
	v_add_f32_e32 v160, v173, v160
	v_add_f32_e32 v160, v174, v160
	v_fmac_f32_e32 v175, v44, v44
	v_add_f32_e32 v160, v175, v160
	ds_bpermute_b32 v161, v58, v160
	s_waitcnt lgkmcnt(0)
	v_add_f32_e32 v160, v160, v161
	ds_bpermute_b32 v161, v59, v160
	s_waitcnt lgkmcnt(0)
	v_add_f32_e32 v160, v160, v161
	ds_bpermute_b32 v161, v60, v160
	s_waitcnt lgkmcnt(0)
	v_add_f32_e32 v160, v160, v161
	ds_bpermute_b32 v161, v61, v160
	s_waitcnt lgkmcnt(0)
	v_add_f32_e32 v160, v160, v161
	ds_bpermute_b32 v161, v62, v160
	s_waitcnt lgkmcnt(0)
	v_add_f32_e32 v160, v160, v161
	ds_bpermute_b32 v161, v63, v160
	s_and_saveexec_b64 s[6:7], s[66:67]
	s_cbranch_execz .LBB0_574
	s_waitcnt lgkmcnt(0)
	v_add_f32_e32 v160, v160, v161
	v_fmamk_f32 v160, v160, 0x3a000000, v69
	v_mul_f32_e32 v161, 0x4b800000, v160
	v_cmp_gt_f32_e32 vcc, s52, v160
	s_nop 1
	v_cndmask_b32_e32 v160, v160, v161, vcc
	v_rsq_f32_e32 v160, v160
	s_nop 0
	v_mul_f32_e32 v161, 0x45800000, v160
	v_cndmask_b32_e32 v160, v160, v161, vcc
	v_mov_b32_e32 v161, s96
	ds_write_b32 v161, v160 offset:4
.LBB0_574:
	s_or_b64 exec, exec, s[6:7]
	s_or_b32 s6, s2, 2
	s_ashr_i32 s7, s6, 31
	s_lshl_b64 s[6:7], s[6:7], 12
	s_waitcnt lgkmcnt(0)
	s_waitcnt vmcnt(7)
	v_lshlrev_b32_e32 v18, 16, v176
	v_and_b32_e32 v176, 0xffff0000, v176
	v_lshlrev_b32_e32 v30, 16, v177
	v_and_b32_e32 v177, 0xffff0000, v177
	v_lshlrev_b32_e32 v31, 16, v178
	v_and_b32_e32 v178, 0xffff0000, v178
	v_mul_f32_e32 v176, v176, v176
	v_mul_f32_e32 v177, v177, v177
	v_lshlrev_b32_e32 v32, 16, v179
	v_and_b32_e32 v179, 0xffff0000, v179
	v_mul_f32_e32 v178, v178, v178
	v_fmac_f32_e32 v176, v18, v18
	v_fmac_f32_e32 v177, v30, v30
	s_waitcnt vmcnt(6)
	v_lshlrev_b32_e32 v33, 16, v180
	v_and_b32_e32 v180, 0xffff0000, v180
	v_mul_f32_e32 v179, v179, v179
	v_fmac_f32_e32 v178, v31, v31
	v_add_f32_e32 v176, v176, v177
	v_lshlrev_b32_e32 v34, 16, v181
	v_and_b32_e32 v181, 0xffff0000, v181
	v_mul_f32_e32 v180, v180, v180
	v_fmac_f32_e32 v179, v32, v32
	v_add_f32_e32 v176, v178, v176
	v_lshlrev_b32_e32 v35, 16, v182
	v_and_b32_e32 v182, 0xffff0000, v182
	v_mul_f32_e32 v181, v181, v181
	v_fmac_f32_e32 v180, v33, v33
	v_add_f32_e32 v176, v179, v176
	v_lshlrev_b32_e32 v36, 16, v183
	v_and_b32_e32 v183, 0xffff0000, v183
	v_mul_f32_e32 v182, v182, v182
	v_fmac_f32_e32 v181, v34, v34
	v_add_f32_e32 v176, v180, v176
	s_waitcnt vmcnt(5)
	v_lshlrev_b32_e32 v37, 16, v184
	v_and_b32_e32 v184, 0xffff0000, v184
	v_mul_f32_e32 v183, v183, v183
	v_fmac_f32_e32 v182, v35, v35
	v_add_f32_e32 v176, v181, v176
	v_lshlrev_b32_e32 v38, 16, v185
	v_and_b32_e32 v185, 0xffff0000, v185
	v_mul_f32_e32 v184, v184, v184
	v_fmac_f32_e32 v183, v36, v36
	v_add_f32_e32 v176, v182, v176
	v_lshlrev_b32_e32 v39, 16, v186
	v_and_b32_e32 v186, 0xffff0000, v186
	v_mul_f32_e32 v185, v185, v185
	v_fmac_f32_e32 v184, v37, v37
	v_add_f32_e32 v176, v183, v176
	v_lshlrev_b32_e32 v40, 16, v187
	v_and_b32_e32 v187, 0xffff0000, v187
	v_mul_f32_e32 v186, v186, v186
	v_fmac_f32_e32 v185, v38, v38
	v_add_f32_e32 v176, v184, v176
	s_waitcnt vmcnt(4)
	v_lshlrev_b32_e32 v41, 16, v188
	v_and_b32_e32 v188, 0xffff0000, v188
	v_mul_f32_e32 v187, v187, v187
	v_fmac_f32_e32 v186, v39, v39
	v_add_f32_e32 v176, v185, v176
	v_lshlrev_b32_e32 v42, 16, v189
	v_and_b32_e32 v189, 0xffff0000, v189
	v_mul_f32_e32 v188, v188, v188
	v_fmac_f32_e32 v187, v40, v40
	v_add_f32_e32 v176, v186, v176
	v_lshlrev_b32_e32 v43, 16, v190
	v_and_b32_e32 v190, 0xffff0000, v190
	v_mul_f32_e32 v189, v189, v189
	v_fmac_f32_e32 v188, v41, v41
	v_add_f32_e32 v176, v187, v176
	v_lshlrev_b32_e32 v44, 16, v191
	v_and_b32_e32 v191, 0xffff0000, v191
	v_mul_f32_e32 v190, v190, v190
	v_fmac_f32_e32 v189, v42, v42
	v_add_f32_e32 v176, v188, v176
	v_mul_f32_e32 v191, v191, v191
	v_fmac_f32_e32 v190, v43, v43
	v_add_f32_e32 v176, v189, v176
	v_add_f32_e32 v176, v190, v176
	v_fmac_f32_e32 v191, v44, v44
	v_add_f32_e32 v176, v191, v176
	ds_bpermute_b32 v177, v58, v176
	s_waitcnt lgkmcnt(0)
	v_add_f32_e32 v176, v176, v177
	ds_bpermute_b32 v177, v59, v176
	s_waitcnt lgkmcnt(0)
	v_add_f32_e32 v176, v176, v177
	ds_bpermute_b32 v177, v60, v176
	s_waitcnt lgkmcnt(0)
	v_add_f32_e32 v176, v176, v177
	ds_bpermute_b32 v177, v61, v176
	s_waitcnt lgkmcnt(0)
	v_add_f32_e32 v176, v176, v177
	ds_bpermute_b32 v177, v62, v176
	s_waitcnt lgkmcnt(0)
	v_add_f32_e32 v176, v176, v177
	ds_bpermute_b32 v177, v63, v176
	s_and_saveexec_b64 s[6:7], s[66:67]
	s_cbranch_execz .LBB0_576
	s_waitcnt lgkmcnt(0)
	v_add_f32_e32 v176, v176, v177
	v_fmamk_f32 v176, v176, 0x3a000000, v69
	v_mul_f32_e32 v177, 0x4b800000, v176
	v_cmp_gt_f32_e32 vcc, s52, v176
	s_nop 1
	v_cndmask_b32_e32 v176, v176, v177, vcc
	v_rsq_f32_e32 v176, v176
	s_nop 0
	v_mul_f32_e32 v177, 0x45800000, v176
	v_cndmask_b32_e32 v176, v176, v177, vcc
	v_mov_b32_e32 v177, s96
	ds_write_b32 v177, v176 offset:8
.LBB0_576:
	s_or_b64 exec, exec, s[6:7]
	s_or_b32 s2, s2, 3
	s_ashr_i32 s3, s2, 31
	s_lshl_b64 s[2:3], s[2:3], 12
	s_waitcnt lgkmcnt(0)
	s_waitcnt vmcnt(3)
	v_lshlrev_b32_e32 v18, 16, v192
	v_and_b32_e32 v192, 0xffff0000, v192
	v_lshlrev_b32_e32 v30, 16, v193
	v_and_b32_e32 v193, 0xffff0000, v193
	v_lshlrev_b32_e32 v31, 16, v194
	v_and_b32_e32 v194, 0xffff0000, v194
	v_mul_f32_e32 v192, v192, v192
	v_mul_f32_e32 v193, v193, v193
	v_lshlrev_b32_e32 v32, 16, v195
	v_and_b32_e32 v195, 0xffff0000, v195
	v_mul_f32_e32 v194, v194, v194
	v_fmac_f32_e32 v192, v18, v18
	v_fmac_f32_e32 v193, v30, v30
	s_waitcnt vmcnt(2)
	v_lshlrev_b32_e32 v33, 16, v196
	v_and_b32_e32 v196, 0xffff0000, v196
	v_mul_f32_e32 v195, v195, v195
	v_fmac_f32_e32 v194, v31, v31
	v_add_f32_e32 v192, v192, v193
	v_lshlrev_b32_e32 v34, 16, v197
	v_and_b32_e32 v197, 0xffff0000, v197
	v_mul_f32_e32 v196, v196, v196
	v_fmac_f32_e32 v195, v32, v32
	v_add_f32_e32 v192, v194, v192
	v_lshlrev_b32_e32 v35, 16, v198
	v_and_b32_e32 v198, 0xffff0000, v198
	v_mul_f32_e32 v197, v197, v197
	v_fmac_f32_e32 v196, v33, v33
	v_add_f32_e32 v192, v195, v192
	v_lshlrev_b32_e32 v36, 16, v199
	v_and_b32_e32 v199, 0xffff0000, v199
	v_mul_f32_e32 v198, v198, v198
	v_fmac_f32_e32 v197, v34, v34
	v_add_f32_e32 v192, v196, v192
	s_waitcnt vmcnt(1)
	v_lshlrev_b32_e32 v37, 16, v200
	v_and_b32_e32 v200, 0xffff0000, v200
	v_mul_f32_e32 v199, v199, v199
	v_fmac_f32_e32 v198, v35, v35
	v_add_f32_e32 v192, v197, v192
	v_lshlrev_b32_e32 v38, 16, v201
	v_and_b32_e32 v201, 0xffff0000, v201
	v_mul_f32_e32 v200, v200, v200
	v_fmac_f32_e32 v199, v36, v36
	v_add_f32_e32 v192, v198, v192
	v_lshlrev_b32_e32 v39, 16, v202
	v_and_b32_e32 v202, 0xffff0000, v202
	v_mul_f32_e32 v201, v201, v201
	v_fmac_f32_e32 v200, v37, v37
	v_add_f32_e32 v192, v199, v192
	v_lshlrev_b32_e32 v40, 16, v203
	v_and_b32_e32 v203, 0xffff0000, v203
	v_mul_f32_e32 v202, v202, v202
	v_fmac_f32_e32 v201, v38, v38
	v_add_f32_e32 v192, v200, v192
	s_waitcnt vmcnt(0)
	v_lshlrev_b32_e32 v41, 16, v204
	v_and_b32_e32 v204, 0xffff0000, v204
	v_mul_f32_e32 v203, v203, v203
	v_fmac_f32_e32 v202, v39, v39
	v_add_f32_e32 v192, v201, v192
	v_lshlrev_b32_e32 v42, 16, v205
	v_and_b32_e32 v205, 0xffff0000, v205
	v_mul_f32_e32 v204, v204, v204
	v_fmac_f32_e32 v203, v40, v40
	v_add_f32_e32 v192, v202, v192
	v_lshlrev_b32_e32 v43, 16, v206
	v_and_b32_e32 v206, 0xffff0000, v206
	v_mul_f32_e32 v205, v205, v205
	v_fmac_f32_e32 v204, v41, v41
	v_add_f32_e32 v192, v203, v192
	v_lshlrev_b32_e32 v44, 16, v207
	v_and_b32_e32 v207, 0xffff0000, v207
	v_mul_f32_e32 v206, v206, v206
	v_fmac_f32_e32 v205, v42, v42
	v_add_f32_e32 v192, v204, v192
	v_mul_f32_e32 v207, v207, v207
	v_fmac_f32_e32 v206, v43, v43
	v_add_f32_e32 v192, v205, v192
	v_add_f32_e32 v192, v206, v192
	v_fmac_f32_e32 v207, v44, v44
	v_add_f32_e32 v192, v207, v192
	ds_bpermute_b32 v193, v58, v192
	s_waitcnt lgkmcnt(0)
	v_add_f32_e32 v192, v192, v193
	ds_bpermute_b32 v193, v59, v192
	s_waitcnt lgkmcnt(0)
	v_add_f32_e32 v192, v192, v193
	ds_bpermute_b32 v193, v60, v192
	s_waitcnt lgkmcnt(0)
	v_add_f32_e32 v192, v192, v193
	ds_bpermute_b32 v193, v61, v192
	s_waitcnt lgkmcnt(0)
	v_add_f32_e32 v192, v192, v193
	ds_bpermute_b32 v193, v62, v192
	s_waitcnt lgkmcnt(0)
	v_add_f32_e32 v192, v192, v193
	ds_bpermute_b32 v193, v63, v192
	s_and_saveexec_b64 s[2:3], s[66:67]
	s_cbranch_execz .LBB0_578
	s_waitcnt lgkmcnt(0)
	v_add_f32_e32 v192, v192, v193
	v_fmamk_f32 v192, v192, 0x3a000000, v69
	v_mul_f32_e32 v193, 0x4b800000, v192
	v_cmp_gt_f32_e32 vcc, s52, v192
	s_nop 1
	v_cndmask_b32_e32 v192, v192, v193, vcc
	v_rsq_f32_e32 v192, v192
	s_nop 0
	v_mul_f32_e32 v193, 0x45800000, v192
	v_cndmask_b32_e32 v192, v192, v193, vcc
	v_mov_b32_e32 v193, s96
	ds_write_b32 v193, v192 offset:12
